# speedup vs baseline: 1.0120x; 1.0088x over previous
.Lk2f_w7x:
	v_add_u32_e32 v19, s5, v18
	v_sub_u32_e32 v19, s38, v19
	ds_read_b128 v[20:23], v16 offset:33712
	v_cmp_lt_i32_e32 vcc, 3, v19
	v_cmp_lt_i32_e64 s[42:43], 0, v19
	v_cmp_lt_i32_e64 s[44:45], 1, v19
	v_cmp_lt_i32_e64 s[46:47], 2, v19
	s_waitcnt lgkmcnt(0)
	s_andn2_b64 s[42:43], s[42:43], vcc
	s_andn2_b64 s[44:45], s[44:45], vcc
	s_andn2_b64 s[46:47], s[46:47], vcc
	s_and_saveexec_b64 s[40:41], vcc
	s_cbranch_execz .Lk2f_w7y0
	global_store_dwordx4 v17, v[20:23], s[16:17] sc1
